# speedup vs baseline: 1.0075x; 1.0019x over previous
_Z10enc_kernelPKfS0_PK15HIP_vector_typeIjLj4EES4_S4_S0_S0_S0_Pf:
	s_load_dwordx4 s[12:15], s[0:1], 0x0
	s_load_dwordx2 s[16:17], s[0:1], 0x10
	s_load_dwordx8 s[4:11], s[0:1], 0x28
	v_lshrrev_b32_e32 v56, 6, v0
	s_lshl_b32 s2, s2, 6
	v_lshl_or_b32 v47, v56, 4, s2
	v_and_b32_e32 v57, 15, v0
	v_or_b32_e32 v2, v47, v57
	v_ashrrev_i32_e32 v3, 31, v2
	s_waitcnt lgkmcnt(0)
	v_and_b32_e32 v119, 48, v0
	global_load_dwordx4 v[120:123], v119, s[4:5]
	global_load_dwordx4 v[124:127], v119, s[4:5] offset:64
	global_load_dwordx4 v[128:131], v119, s[4:5] offset:128
	global_load_dwordx4 v[132:135], v119, s[4:5] offset:192
	global_load_dwordx4 v[136:139], v119, s[4:5] offset:256
	global_load_dwordx4 v[140:143], v119, s[4:5] offset:320
	global_load_dwordx4 v[144:147], v119, s[4:5] offset:384
	global_load_dwordx4 v[148:151], v119, s[4:5] offset:448
	global_load_dwordx4 a[0:3], v119, s[6:7]
	global_load_dwordx4 a[56:59], v119, s[6:7] offset:64
	global_load_dwordx4 a[4:7], v119, s[6:7] offset:128
	global_load_dwordx4 v[164:167], v119, s[6:7] offset:192
	global_load_dwordx4 a[32:35], v119, s[6:7] offset:256
	global_load_dwordx4 a[40:43], v119, s[6:7] offset:320
	global_load_dwordx4 a[8:11], v119, s[8:9]
	global_load_dwordx4 v[180:183], v119, s[8:9] offset:64
	global_load_dwordx4 a[12:15], v119, s[8:9] offset:128
	global_load_dwordx4 v[188:191], v119, s[8:9] offset:192
	v_lshl_add_u64 v[4:5], v[2:3], 2, s[14:15]
	global_load_dword v46, v[4:5], off
	v_mov_b32_e32 v45, 0
	v_lshlrev_b64 v[2:3], 9, v[2:3]
	v_lshlrev_b32_e32 v44, 4, v0
	v_lshl_add_u64 v[2:3], s[12:13], 0, v[2:3]
	v_and_b32_e32 v48, 48, v0
	v_mov_b32_e32 v49, v45
	v_lshl_add_u64 v[4:5], s[16:17], 0, v[44:45]
	v_lshl_add_u64 v[42:43], v[2:3], 0, v[48:49]
	s_movk_i32 s0, 0x2000
	v_add_co_u32_e32 v2, vcc, s0, v4
	s_movk_i32 s0, 0x4000
	s_nop 0
	v_addc_co_u32_e32 v3, vcc, 0, v5, vcc
	v_add_co_u32_e32 v6, vcc, s0, v4
	s_movk_i32 s0, 0x6000
	s_nop 0
	v_addc_co_u32_e32 v7, vcc, 0, v5, vcc
	global_load_dwordx4 v[18:21], v44, s[16:17]
	global_load_dwordx4 v[22:25], v[2:3], off offset:-4096
	global_load_dwordx4 v[26:29], v[2:3], off
	global_load_dwordx4 v[30:33], v[6:7], off offset:-4096
	v_add_co_u32_e32 v2, vcc, s0, v4
	s_mov_b32 s0, 0x8000
	s_nop 0
	v_addc_co_u32_e32 v3, vcc, 0, v5, vcc
	global_load_dwordx4 v[34:37], v[6:7], off
	global_load_dwordx4 v[38:41], v[2:3], off offset:-4096
	v_add_co_u32_e32 v6, vcc, s0, v4
	s_mov_b32 s0, 0xa000
	s_nop 0
	v_addc_co_u32_e32 v7, vcc, 0, v5, vcc
	global_load_dwordx4 v[50:53], v[2:3], off
	global_load_dwordx4 v[58:61], v[6:7], off offset:-4096
	v_add_co_u32_e32 v2, vcc, s0, v4
	s_mov_b32 s0, 0xc000
	s_nop 0
	v_addc_co_u32_e32 v3, vcc, 0, v5, vcc
	global_load_dwordx4 v[62:65], v[6:7], off
	global_load_dwordx4 v[66:69], v[2:3], off offset:-4096
	v_add_co_u32_e32 v6, vcc, s0, v4
	s_mov_b32 s0, 0xe000
	s_nop 0
	v_addc_co_u32_e32 v7, vcc, 0, v5, vcc
	global_load_dwordx4 v[70:73], v[2:3], off
	global_load_dwordx4 v[74:77], v[6:7], off offset:-4096
	v_add_co_u32_e32 v2, vcc, s0, v4
	s_mov_b32 s0, 0x10000
	s_nop 0
	v_addc_co_u32_e32 v3, vcc, 0, v5, vcc
	v_add_co_u32_e32 v4, vcc, s0, v4
	global_load_dwordx4 v[78:81], v[6:7], off
	global_load_dwordx4 v[82:85], v[2:3], off offset:-4096
	v_addc_co_u32_e32 v5, vcc, 0, v5, vcc
	global_load_dwordx4 v[86:89], v[2:3], off
	global_load_dwordx4 v[90:93], v[4:5], off offset:-4096
	global_load_dwordx4 v[94:97], v[4:5], off
	global_load_dwordx4 v[98:101], v[42:43], off
	global_load_dwordx4 v[102:105], v[42:43], off offset:64
	global_load_dwordx4 v[106:109], v[42:43], off offset:128
	global_load_dwordx4 v[110:113], v[42:43], off offset:192
	global_load_dwordx4 v[10:13], v[42:43], off offset:256
	global_load_dwordx4 v[14:17], v[42:43], off offset:320
	s_nop 0
	global_load_dwordx4 v[2:5], v[42:43], off offset:384
	global_load_dwordx4 v[6:9], v[42:43], off offset:448
	v_or_b32_e32 v1, 0x10000, v44
	v_and_b32_e32 v49, 63, v0
	s_movk_i32 s0, 0x1040
	s_movk_i32 s2, 0x104
	v_cmp_gt_u32_e32 vcc, 16, v49
	s_waitcnt vmcnt(24)
	ds_write_b128 v44, v[18:21]
	s_waitcnt vmcnt(23)
	ds_write_b128 v44, v[22:25] offset:4096
	s_waitcnt vmcnt(22)
	ds_write_b128 v44, v[26:29] offset:8192
	s_waitcnt vmcnt(21)
	ds_write_b128 v44, v[30:33] offset:12288
	s_waitcnt vmcnt(20)
	ds_write_b128 v44, v[34:37] offset:16384
	s_waitcnt vmcnt(19)
	ds_write_b128 v44, v[38:41] offset:20480
	s_waitcnt vmcnt(18)
	ds_write_b128 v44, v[50:53] offset:24576
	s_waitcnt vmcnt(17)
	ds_write_b128 v44, v[58:61] offset:28672
	s_waitcnt vmcnt(16)
	ds_write_b128 v44, v[62:65] offset:32768
	s_waitcnt vmcnt(15)
	ds_write_b128 v44, v[66:69] offset:36864
	s_waitcnt vmcnt(14)
	ds_write_b128 v44, v[70:73] offset:40960
	s_waitcnt vmcnt(13)
	ds_write_b128 v44, v[74:77] offset:45056
	s_waitcnt vmcnt(12)
	ds_write_b128 v44, v[78:81] offset:49152
	s_waitcnt vmcnt(11)
	ds_write_b128 v44, v[82:85] offset:53248
	s_waitcnt vmcnt(10)
	ds_write_b128 v44, v[86:89] offset:57344
	s_waitcnt vmcnt(9)
	ds_write_b128 v44, v[90:93] offset:61440
	s_waitcnt vmcnt(8)
	ds_write_b128 v1, v[94:97]
	s_waitcnt lgkmcnt(0)
	s_barrier
	s_waitcnt vmcnt(0)
	v_pk_fma_f32 v[18:19], v[98:99], -2.0, v[46:47] op_sel_hi:[1,0,0]
	v_pk_fma_f32 v[20:21], v[100:101], -2.0, v[46:47] op_sel_hi:[1,0,0]
	v_pk_fma_f32 v[22:23], v[102:103], -2.0, v[46:47] op_sel_hi:[1,0,0]
	v_pk_fma_f32 v[36:37], v[104:105], -2.0, v[46:47] op_sel_hi:[1,0,0]
	v_pk_fma_f32 v[38:39], v[106:107], -2.0, v[46:47] op_sel_hi:[1,0,0]
	v_cvt_pk_bf16_f32 v18, v18, v19
	v_cvt_pk_bf16_f32 v19, v20, v21
	v_cvt_pk_bf16_f32 v20, v22, v23
	v_cvt_pk_bf16_f32 v21, v36, v37
	v_cvt_pk_bf16_f32 v22, v38, v39
	v_lshlrev_b32_e32 v44, 4, v49
	ds_read_b128 v[58:61], v44
	ds_read_b128 v[62:65], v44 offset:1024
	ds_read_b128 v[66:69], v44 offset:4096
	ds_read_b128 v[70:73], v44 offset:5120
	ds_read_b128 v[74:77], v44 offset:8192
	ds_read_b128 v[78:81], v44 offset:9216
	ds_read_b128 v[82:85], v44 offset:12288
	ds_read_b128 v[86:89], v44 offset:13312
	v_pk_fma_f32 v[50:51], v[108:109], -2.0, v[46:47] op_sel_hi:[1,0,0]
	v_pk_fma_f32 v[52:53], v[110:111], -2.0, v[46:47] op_sel_hi:[1,0,0]
	v_pk_fma_f32 v[54:55], v[112:113], -2.0, v[46:47] op_sel_hi:[1,0,0]
	v_cvt_pk_bf16_f32 v23, v50, v51
	v_pk_fma_f32 v[0:1], v[10:11], -2.0, v[46:47] op_sel_hi:[1,0,0]
	v_pk_fma_f32 v[12:13], v[12:13], -2.0, v[46:47] op_sel_hi:[1,0,0]
	v_cvt_pk_bf16_f32 v10, v0, v1
	v_cvt_pk_bf16_f32 v11, v12, v13
	v_pk_fma_f32 v[8:9], v[8:9], -2.0, v[46:47] op_sel_hi:[1,0,0]
	v_pk_mul_f32 v[24:25], v[46:47], v[120:121] op_sel_hi:[0,1]
	v_pk_mul_f32 v[26:27], v[46:47], v[122:123] op_sel_hi:[0,1]
	v_accvgpr_write_b32 a16, v24
	v_accvgpr_write_b32 a17, v25
	v_accvgpr_write_b32 a18, v26
	v_accvgpr_write_b32 a19, v27
	v_pk_mul_f32 v[24:25], v[46:47], v[124:125] op_sel_hi:[0,1]
	v_pk_mul_f32 v[26:27], v[46:47], v[126:127] op_sel_hi:[0,1]
	v_accvgpr_write_b32 a20, v24
	v_accvgpr_write_b32 a21, v25
	v_accvgpr_write_b32 a22, v26
	v_accvgpr_write_b32 a23, v27
	v_pk_mul_f32 v[24:25], v[46:47], v[128:129] op_sel_hi:[0,1]
	v_pk_mul_f32 v[26:27], v[46:47], v[130:131] op_sel_hi:[0,1]
	v_accvgpr_write_b32 a24, v24
	v_accvgpr_write_b32 a25, v25
	v_accvgpr_write_b32 a26, v26
	v_accvgpr_write_b32 a27, v27
	v_pk_mul_f32 v[26:27], v[46:47], v[134:135] op_sel_hi:[0,1]
	v_pk_mul_f32 v[24:25], v[46:47], v[132:133] op_sel_hi:[0,1]
	v_accvgpr_write_b32 a31, v27
	v_accvgpr_write_b32 a30, v26
	v_accvgpr_write_b32 a29, v25
	v_accvgpr_write_b32 a28, v24
	v_pk_fma_f32 v[26:27], v[14:15], -2.0, v[46:47] op_sel_hi:[1,0,0]
	v_pk_fma_f32 v[28:29], v[16:17], -2.0, v[46:47] op_sel_hi:[1,0,0]
	ds_read_b128 v[14:17], v44 offset:2048
	s_waitcnt lgkmcnt(8)
	v_mfma_f32_16x16x32_bf16 a[16:19], v[58:61], v[18:21], a[16:19]
	v_cvt_pk_bf16_f32 v24, v52, v53
	v_cvt_pk_bf16_f32 v25, v54, v55
	v_cvt_pk_bf16_f32 v12, v26, v27
	s_waitcnt lgkmcnt(2)
	v_mfma_f32_16x16x32_bf16 a[28:31], v[82:85], v[18:21], a[28:31]
	v_cvt_pk_bf16_f32 v13, v28, v29
	ds_read_b128 v[26:29], v44 offset:6144
	ds_read_b128 v[40:43], v44 offset:3072
	ds_read_b128 v[50:53], v44 offset:10240
	v_mfma_f32_16x16x32_bf16 a[16:19], v[62:65], v[22:25], a[16:19]
	v_fma_f32 v34, v2, -2.0, v46
	v_fma_f32 v35, v3, -2.0, v46
	v_pk_fma_f32 v[54:55], v[6:7], -2.0, v[46:47] op_sel_hi:[1,0,0]
	v_pk_mul_f32 v[32:33], v[46:47], v[142:143] op_sel_hi:[0,1]
	s_waitcnt lgkmcnt(3)
	v_mfma_f32_16x16x32_bf16 a[16:19], v[14:17], v[10:13], a[16:19]
	ds_read_b128 v[0:3], v44 offset:7168
	ds_read_b128 v[14:17], v44 offset:14336
	v_pk_mul_f32 v[30:31], v[46:47], v[140:141] op_sel_hi:[0,1]
	v_accvgpr_write_b32 a47, v33
	v_mfma_f32_16x16x32_bf16 a[28:31], v[86:89], v[22:25], a[28:31]
	v_accvgpr_write_b32 a46, v32
	v_accvgpr_write_b32 a45, v31
	v_accvgpr_write_b32 a44, v30
	s_waitcnt lgkmcnt(0)
	v_mfma_f32_16x16x32_bf16 a[28:31], v[14:17], v[10:13], a[28:31]
	s_nop 1
	ds_read_b128 v[30:33], v44 offset:23552
	v_mfma_f32_16x16x32_bf16 a[20:23], v[66:69], v[18:21], a[20:23]
	v_mfma_f32_16x16x32_bf16 a[20:23], v[70:73], v[22:25], a[20:23]
	v_mfma_f32_16x16x32_bf16 a[20:23], v[26:29], v[10:13], a[20:23]
	v_fma_f32 v28, v4, -2.0, v46
	v_fma_f32 v29, v5, -2.0, v46
	v_cvt_pk_bf16_f32 v26, v34, v35
	v_cvt_pk_bf16_f32 v27, v28, v29
	v_cvt_pk_bf16_f32 v28, v54, v55
	v_cvt_pk_bf16_f32 v29, v8, v9
	v_mfma_f32_16x16x32_bf16 a[24:27], v[74:77], v[18:21], a[24:27]
	ds_read_b128 v[4:7], v44 offset:11264
	v_pk_mul_f32 v[34:35], v[46:47], v[136:137] op_sel_hi:[0,1]
	v_pk_mul_f32 v[36:37], v[46:47], v[138:139] op_sel_hi:[0,1]
	v_mfma_f32_16x16x32_bf16 a[20:23], v[0:3], v[26:29], a[20:23]
	s_nop 1
	v_accvgpr_write_b32 a39, v37
	v_accvgpr_write_b32 a38, v36
	v_mfma_f32_16x16x32_bf16 a[24:27], v[78:81], v[22:25], a[24:27]
	v_accvgpr_write_b32 a37, v35
	v_accvgpr_write_b32 a36, v34
	ds_read_b128 v[34:37], v44 offset:19456
	v_mfma_f32_16x16x32_bf16 a[24:27], v[50:53], v[10:13], a[24:27]
	ds_read_b128 v[50:53], v44 offset:15360
	v_pk_mul_f32 v[16:17], v[46:47], v[146:147] op_sel_hi:[0,1]
	s_waitcnt lgkmcnt(2)
	v_mfma_f32_16x16x32_bf16 a[24:27], v[4:7], v[26:29], a[24:27]
	ds_read_b128 v[4:7], v44 offset:16384
	v_pk_mul_f32 v[14:15], v[46:47], v[144:145] op_sel_hi:[0,1]
	v_accvgpr_write_b32 a51, v17
	v_mfma_f32_16x16x32_bf16 a[16:19], v[40:43], v[26:29], a[16:19]
	ds_read_b128 v[40:43], v44 offset:17408
	v_accvgpr_write_b32 a50, v16
	v_accvgpr_write_b32 a49, v15
	s_waitcnt lgkmcnt(1)
	v_mfma_f32_16x16x32_bf16 a[36:39], v[4:7], v[18:21], a[36:39]
	ds_read_b128 v[4:7], v44 offset:18432
	v_accvgpr_write_b32 a48, v14
	ds_read_b128 v[14:17], v44 offset:27648
	s_waitcnt lgkmcnt(2)
	v_mfma_f32_16x16x32_bf16 a[36:39], v[40:43], v[22:25], a[36:39]
	v_pk_mul_f32 v[2:3], v[46:47], v[150:151] op_sel_hi:[0,1]
	s_waitcnt lgkmcnt(1)
	v_mfma_f32_16x16x32_bf16 a[36:39], v[4:7], v[10:13], a[36:39]
	ds_read_b128 v[4:7], v44 offset:20480
	v_pk_mul_f32 v[0:1], v[46:47], v[148:149] op_sel_hi:[0,1]
	v_accvgpr_write_b32 a55, v3
	v_mfma_f32_16x16x32_bf16 a[36:39], v[34:37], v[26:29], a[36:39]
	ds_read_b128 v[34:37], v44 offset:21504
	v_accvgpr_write_b32 a54, v2
	v_accvgpr_write_b32 a53, v1
	s_waitcnt lgkmcnt(1)
	v_mfma_f32_16x16x32_bf16 a[44:47], v[4:7], v[18:21], a[44:47]
	ds_read_b128 v[4:7], v44 offset:22528
	v_accvgpr_write_b32 a52, v0
	ds_read_b128 v[0:3], v44 offset:30720
	s_waitcnt lgkmcnt(2)
	v_mfma_f32_16x16x32_bf16 a[44:47], v[34:37], v[22:25], a[44:47]
	v_accvgpr_read_b32 v9, a36
	s_waitcnt lgkmcnt(1)
	v_mfma_f32_16x16x32_bf16 a[44:47], v[4:7], v[10:13], a[44:47]
	ds_read_b128 v[4:7], v44 offset:24576
	v_mfma_f32_16x16x32_bf16 a[44:47], v[30:33], v[26:29], a[44:47]
	ds_read_b128 v[30:33], v44 offset:25600
	s_waitcnt lgkmcnt(1)
	v_mfma_f32_16x16x32_bf16 a[48:51], v[4:7], v[18:21], a[48:51]
	ds_read_b128 v[4:7], v44 offset:26624
	s_waitcnt lgkmcnt(1)
	v_mfma_f32_16x16x32_bf16 a[48:51], v[30:33], v[22:25], a[48:51]
	s_waitcnt lgkmcnt(0)
	v_mfma_f32_16x16x32_bf16 a[48:51], v[4:7], v[10:13], a[48:51]
	ds_read_b128 v[4:7], v44 offset:28672
	v_mfma_f32_16x16x32_bf16 a[48:51], v[14:17], v[26:29], a[48:51]
	ds_read_b128 v[14:17], v44 offset:29696
	s_waitcnt lgkmcnt(1)
	v_mfma_f32_16x16x32_bf16 a[52:55], v[4:7], v[18:21], a[52:55]
	ds_read_b128 v[4:7], v44 offset:31744
	s_nop 3
	v_accvgpr_read_b32 v20, a49
	s_waitcnt lgkmcnt(1)
	v_mfma_f32_16x16x32_bf16 a[52:55], v[14:17], v[22:25], a[52:55]
	v_accvgpr_read_b32 v16, a46
	v_accvgpr_read_b32 v21, a48
	v_cvt_pk_bf16_f32 v20, v21, v20
	v_mfma_f32_16x16x32_bf16 a[52:55], v[0:3], v[10:13], a[52:55]
	v_accvgpr_read_b32 v0, a17
	v_accvgpr_read_b32 v1, a16
	v_cvt_pk_bf16_f32 v0, v1, v0
	v_accvgpr_read_b32 v1, a19
	v_accvgpr_read_b32 v2, a18
	v_mfma_f32_16x16x32_bf16 a[28:31], v[50:53], v[26:29], a[28:31]
	v_cvt_pk_bf16_f32 v1, v2, v1
	v_accvgpr_read_b32 v2, a21
	v_accvgpr_read_b32 v3, a20
	s_waitcnt lgkmcnt(0)
	v_mfma_f32_16x16x32_bf16 a[52:55], v[4:7], v[26:29], a[52:55]
	v_cvt_pk_bf16_f32 v2, v3, v2
	v_accvgpr_read_b32 v3, a23
	v_accvgpr_read_b32 v4, a22
	v_cvt_pk_bf16_f32 v3, v4, v3
	v_accvgpr_read_b32 v4, a25
	v_accvgpr_read_b32 v5, a24
	v_cvt_pk_bf16_f32 v4, v5, v4
	v_accvgpr_read_b32 v5, a27
	v_accvgpr_read_b32 v6, a26
	v_cvt_pk_bf16_f32 v5, v6, v5
	v_accvgpr_read_b32 v6, a29
	v_accvgpr_read_b32 v7, a28
	v_cvt_pk_bf16_f32 v6, v7, v6
	v_accvgpr_read_b32 v7, a31
	v_accvgpr_read_b32 v8, a30
	v_cvt_pk_bf16_f32 v7, v8, v7
	v_accvgpr_read_b32 v8, a37
	ds_read_b128 v[12:15], v44 offset:32768
	v_cvt_pk_bf16_f32 v8, v9, v8
	v_accvgpr_read_b32 v9, a39
	v_accvgpr_read_b32 v10, a38
	v_cvt_pk_bf16_f32 v9, v10, v9
	v_accvgpr_read_b32 v10, a45
	v_accvgpr_read_b32 v11, a44
	v_cvt_pk_bf16_f32 v10, v11, v10
	v_accvgpr_read_b32 v11, a47
	v_cvt_pk_bf16_f32 v11, v16, v11
	ds_read_b128 v[16:19], v44 offset:33792
	ds_read_b128 v[24:27], v44 offset:34816
	s_waitcnt lgkmcnt(2)
	v_mfma_f32_16x16x32_bf16 a[0:3], v[12:15], v[0:3], a[0:3]
	v_accvgpr_read_b32 v21, a51
	v_accvgpr_read_b32 v12, a50
	v_cvt_pk_bf16_f32 v21, v12, v21
	ds_read_b128 v[12:15], v44 offset:35840
	s_waitcnt lgkmcnt(2)
	v_mfma_f32_16x16x32_bf16 a[0:3], v[16:19], v[4:7], a[0:3]
	v_accvgpr_read_b32 v16, a53
	v_accvgpr_read_b32 v17, a52
	v_cvt_pk_bf16_f32 v22, v17, v16
	s_waitcnt lgkmcnt(1)
	v_mfma_f32_16x16x32_bf16 a[0:3], v[24:27], v[8:11], a[0:3]
	v_accvgpr_read_b32 v16, a55
	v_accvgpr_read_b32 v17, a54
	v_accvgpr_write_b32 a16, v164
	v_accvgpr_write_b32 a17, v165
	v_accvgpr_write_b32 a18, v166
	v_accvgpr_write_b32 a19, v167
	v_cvt_pk_bf16_f32 v23, v17, v16
	v_accvgpr_write_b32 a20, v180
	v_accvgpr_write_b32 a21, v181
	v_accvgpr_write_b32 a22, v182
	v_accvgpr_write_b32 a23, v183
	s_waitcnt lgkmcnt(0)
	v_mfma_f32_16x16x32_bf16 a[0:3], v[12:15], v[20:23], a[0:3]
	s_nop 7
	v_accvgpr_read_b32 v12, a0
	v_mul_f32_e32 v12, 0x4038aa3b, v12
	v_exp_f32_e32 v16, v12
	v_accvgpr_read_b32 v12, a1
	v_mul_f32_e32 v12, 0x4038aa3b, v12
	v_exp_f32_e32 v17, v12
	ds_read_b128 v[12:15], v44 offset:36864
	v_add_f32_e32 v16, 1.0, v16
	v_rcp_f32_e32 v28, v16
	v_add_f32_e32 v24, 1.0, v17
	ds_read_b128 v[16:19], v44 offset:37888
	v_rcp_f32_e32 v29, v24
	ds_read_b128 v[24:27], v44 offset:38912
	s_waitcnt lgkmcnt(2)
	v_mfma_f32_16x16x32_bf16 a[24:27], v[12:15], v[0:3], a[56:59]
	v_accvgpr_read_b32 v30, a2
	v_mul_f32_e32 v12, 0x4038aa3b, v30
	v_exp_f32_e32 v30, v12
	ds_read_b128 v[12:15], v44 offset:39936
	s_waitcnt lgkmcnt(2)
	v_mfma_f32_16x16x32_bf16 a[24:27], v[16:19], v[4:7], a[24:27]
	v_accvgpr_read_b32 v16, a3
	v_mul_f32_e32 v16, 0x4038aa3b, v16
	v_exp_f32_e32 v17, v16
	s_waitcnt lgkmcnt(1)
	v_mfma_f32_16x16x32_bf16 a[0:3], v[24:27], v[8:11], a[24:27]
	v_add_f32_e32 v16, 1.0, v30
	v_rcp_f32_e32 v16, v16
	v_add_f32_e32 v17, 1.0, v17
	s_waitcnt lgkmcnt(0)
	v_mfma_f32_16x16x32_bf16 a[0:3], v[12:15], v[20:23], a[0:3]
	v_rcp_f32_e32 v17, v17
	v_pk_fma_f32 v[28:29], v[28:29], -2.0, 1.0 op_sel_hi:[1,0,0]
	v_pk_fma_f32 v[30:31], v[16:17], -2.0, 1.0 op_sel_hi:[1,0,0]
	s_nop 4
	v_accvgpr_read_b32 v12, a0
	v_mul_f32_e32 v12, 0x4038aa3b, v12
	v_accvgpr_read_b32 v13, a1
	v_exp_f32_e32 v12, v12
	v_mul_f32_e32 v13, 0x4038aa3b, v13
	v_exp_f32_e32 v13, v13
	v_accvgpr_read_b32 v35, a3
	v_add_f32_e32 v12, 1.0, v12
	v_rcp_f32_e32 v24, v12
	v_add_f32_e32 v18, 1.0, v13
	ds_read_b128 v[12:15], v44 offset:40960
	v_rcp_f32_e32 v25, v18
	ds_read_b128 v[16:19], v44 offset:41984
	s_waitcnt lgkmcnt(1)
	v_mfma_f32_16x16x32_bf16 a[4:7], v[12:15], v[0:3], a[4:7]
	v_fma_f32 v32, v24, -2.0, 1.0
	v_fma_f32 v33, v25, -2.0, 1.0
	v_accvgpr_read_b32 v24, a2
	v_mul_f32_e32 v34, 0x4038aa3b, v24
	ds_read_b128 v[24:27], v44 offset:43008
	ds_read_b128 v[12:15], v44 offset:44032
	s_waitcnt lgkmcnt(2)
	v_mfma_f32_16x16x32_bf16 a[0:3], v[16:19], v[4:7], a[4:7]
	v_mul_f32_e32 v16, 0x4038aa3b, v35
	v_exp_f32_e32 v16, v16
	v_exp_f32_e32 v34, v34
	s_waitcnt lgkmcnt(1)
	v_mfma_f32_16x16x32_bf16 a[0:3], v[24:27], v[8:11], a[0:3]
	v_add_f32_e32 v16, 1.0, v16
	v_rcp_f32_e32 v35, v16
	v_add_f32_e32 v17, 1.0, v34
	s_waitcnt lgkmcnt(0)
	v_mfma_f32_16x16x32_bf16 a[0:3], v[12:15], v[20:23], a[0:3]
	v_rcp_f32_e32 v34, v17
	v_accvgpr_write_b32 a4, v188
	v_accvgpr_write_b32 a5, v189
	v_accvgpr_write_b32 a6, v190
	v_accvgpr_write_b32 a7, v191
	v_pk_fma_f32 v[34:35], v[34:35], -2.0, 1.0 op_sel_hi:[1,0,0]
	s_nop 4
	v_accvgpr_read_b32 v12, a0
	v_mul_f32_e32 v12, 0x4038aa3b, v12
	v_exp_f32_e32 v16, v12
	v_accvgpr_read_b32 v12, a1
	v_mul_f32_e32 v12, 0x4038aa3b, v12
	v_exp_f32_e32 v17, v12
	ds_read_b128 v[12:15], v44 offset:45056
	v_add_f32_e32 v16, 1.0, v16
	v_rcp_f32_e32 v36, v16
	v_add_f32_e32 v24, 1.0, v17
	ds_read_b128 v[16:19], v44 offset:46080
	v_rcp_f32_e32 v37, v24
	ds_read_b128 v[24:27], v44 offset:47104
	s_waitcnt lgkmcnt(2)
	v_mfma_f32_16x16x32_bf16 a[16:19], v[12:15], v[0:3], a[16:19]
	v_accvgpr_read_b32 v38, a2
	v_mul_f32_e32 v12, 0x4038aa3b, v38
	v_exp_f32_e32 v38, v12
	ds_read_b128 v[12:15], v44 offset:48128
	s_waitcnt lgkmcnt(2)
	v_mfma_f32_16x16x32_bf16 a[16:19], v[16:19], v[4:7], a[16:19]
	v_accvgpr_read_b32 v17, a3
	v_mul_f32_e32 v17, 0x4038aa3b, v17
	v_exp_f32_e32 v17, v17
	s_waitcnt lgkmcnt(1)
	v_mfma_f32_16x16x32_bf16 a[16:19], v[24:27], v[8:11], a[16:19]
	v_add_f32_e32 v16, 1.0, v38
	v_rcp_f32_e32 v38, v16
	v_pk_fma_f32 v[36:37], v[36:37], -2.0, 1.0 op_sel_hi:[1,0,0]
	s_waitcnt lgkmcnt(0)
	v_mfma_f32_16x16x32_bf16 a[0:3], v[12:15], v[20:23], a[16:19]
	v_add_f32_e32 v13, 1.0, v17
	v_rcp_f32_e32 v39, v13
	s_nop 0
	v_pk_fma_f32 v[38:39], v[38:39], -2.0, 1.0 op_sel_hi:[1,0,0]
	s_nop 3
	v_accvgpr_read_b32 v12, a0
	v_mul_f32_e32 v12, 0x4038aa3b, v12
	v_exp_f32_e32 v12, v12
	v_accvgpr_read_b32 v17, a2
	v_mul_f32_e32 v17, 0x4038aa3b, v17
	v_exp_f32_e32 v24, v17
	v_add_f32_e32 v12, 1.0, v12
	v_rcp_f32_e32 v40, v12
	v_accvgpr_read_b32 v12, a1
	v_mul_f32_e32 v12, 0x4038aa3b, v12
	v_exp_f32_e32 v16, v12
	ds_read_b128 v[12:15], v44 offset:49152
	v_add_f32_e32 v42, 1.0, v24
	v_accvgpr_read_b32 v43, a3
	v_add_f32_e32 v25, 1.0, v16
	ds_read_b128 v[16:19], v44 offset:50176
	v_rcp_f32_e32 v41, v25
	ds_read_b128 v[24:27], v44 offset:51200
	s_waitcnt lgkmcnt(2)
	v_mfma_f32_16x16x32_bf16 a[0:3], v[12:15], v[0:3], a[32:35]
	v_mul_f32_e32 v12, 0x4038aa3b, v43
	v_exp_f32_e32 v43, v12
	ds_read_b128 v[12:15], v44 offset:52224
	s_waitcnt lgkmcnt(2)
	v_mfma_f32_16x16x32_bf16 a[0:3], v[16:19], v[4:7], a[0:3]
	v_rcp_f32_e32 v16, v42
	v_add_f32_e32 v17, 1.0, v43
	v_rcp_f32_e32 v17, v17
	s_waitcnt lgkmcnt(1)
	v_mfma_f32_16x16x32_bf16 a[0:3], v[24:27], v[8:11], a[0:3]
	v_fma_f32 v40, v40, -2.0, 1.0
	v_fma_f32 v41, v41, -2.0, 1.0
	v_pk_fma_f32 v[42:43], v[16:17], -2.0, 1.0 op_sel_hi:[1,0,0]
	s_waitcnt lgkmcnt(0)
	v_mfma_f32_16x16x32_bf16 a[0:3], v[12:15], v[20:23], a[0:3]
	s_nop 7
	v_accvgpr_read_b32 v12, a0
	v_mul_f32_e32 v12, 0x4038aa3b, v12
	v_exp_f32_e32 v16, v12
	v_accvgpr_read_b32 v12, a1
	v_mul_f32_e32 v17, 0x4038aa3b, v12
	ds_read_b128 v[12:15], v44 offset:53248
	v_exp_f32_e32 v24, v17
	v_add_f32_e32 v16, 1.0, v16
	v_rcp_f32_e32 v50, v16
	ds_read_b128 v[16:19], v44 offset:54272
	v_add_f32_e32 v24, 1.0, v24
	v_rcp_f32_e32 v51, v24
	ds_read_b128 v[24:27], v44 offset:55296
	s_waitcnt lgkmcnt(2)
	v_mfma_f32_16x16x32_bf16 a[16:19], v[12:15], v[0:3], a[40:43]
	v_accvgpr_read_b32 v52, a2
	v_mul_f32_e32 v0, 0x4038aa3b, v52
	v_exp_f32_e32 v12, v0
	ds_read_b128 v[0:3], v44 offset:56320
	s_waitcnt lgkmcnt(2)
	v_mfma_f32_16x16x32_bf16 a[16:19], v[16:19], v[4:7], a[16:19]
	v_accvgpr_read_b32 v4, a3
	v_mul_f32_e32 v4, 0x4038aa3b, v4
	v_exp_f32_e32 v5, v4
	s_waitcnt lgkmcnt(1)
	v_mfma_f32_16x16x32_bf16 a[0:3], v[24:27], v[8:11], a[16:19]
	v_add_f32_e32 v4, 1.0, v12
	ds_read_b128 v[10:13], v44 offset:57344
	v_add_f32_e32 v5, 1.0, v5
	s_waitcnt lgkmcnt(1)
	v_mfma_f32_16x16x32_bf16 a[0:3], v[0:3], v[20:23], a[0:3]
	v_rcp_f32_e32 v4, v4
	v_rcp_f32_e32 v5, v5
	ds_read_b128 v[18:21], v44 offset:58368
	v_pk_fma_f32 v[14:15], v[50:51], -2.0, 1.0 op_sel_hi:[1,0,0]
	v_cvt_pk_bf16_f32 v6, v36, v37
	v_pk_fma_f32 v[16:17], v[4:5], -2.0, 1.0 op_sel_hi:[1,0,0]
	v_cvt_pk_bf16_f32 v4, v32, v33
	v_cvt_pk_bf16_f32 v5, v34, v35
	v_accvgpr_read_b32 v2, a2
	v_accvgpr_read_b32 v3, a3
	v_mul_f32_e32 v2, 0x4038aa3b, v2
	v_mul_f32_e32 v3, 0x4038aa3b, v3
	v_exp_f32_e32 v2, v2
	v_exp_f32_e32 v3, v3
	v_accvgpr_read_b32 v0, a0
	v_accvgpr_read_b32 v1, a1
	v_add_f32_e32 v2, 1.0, v2
	v_add_f32_e32 v3, 1.0, v3
	v_rcp_f32_e32 v2, v2
	v_rcp_f32_e32 v3, v3
	v_mul_f32_e32 v0, 0x4038aa3b, v0
	v_mul_f32_e32 v1, 0x4038aa3b, v1
	v_exp_f32_e32 v0, v0
	v_exp_f32_e32 v1, v1
	v_pk_fma_f32 v[22:23], v[2:3], -2.0, 1.0 op_sel_hi:[1,0,0]
	v_cvt_pk_bf16_f32 v2, v28, v29
	v_cvt_pk_bf16_f32 v3, v30, v31
	v_cvt_pk_bf16_f32 v14, v14, v15
	v_cvt_pk_bf16_f32 v15, v16, v17
	v_cvt_pk_bf16_f32 v17, v22, v23
	ds_read_b128 v[22:25], v44 offset:59392
	s_waitcnt lgkmcnt(2)
	v_mfma_f32_16x16x32_bf16 a[0:3], v[10:13], v[2:5], a[8:11]
	ds_read_b128 v[10:13], v44 offset:60416
	v_add_f32_e32 v0, 1.0, v0
	v_add_f32_e32 v1, 1.0, v1
	v_rcp_f32_e32 v0, v0
	v_rcp_f32_e32 v1, v1
	v_cvt_pk_bf16_f32 v7, v38, v39
	v_cvt_pk_bf16_f32 v8, v40, v41
	v_cvt_pk_bf16_f32 v9, v42, v43
	v_pk_fma_f32 v[0:1], v[0:1], -2.0, 1.0 op_sel_hi:[1,0,0]
	s_waitcnt lgkmcnt(0)
	v_mfma_f32_16x16x32_bf16 a[8:11], v[10:13], v[2:5], a[20:23]
	v_cvt_pk_bf16_f32 v16, v0, v1
	v_mov_b32_e32 v0, 0x11000
	v_mad_u32_u24 v0, v56, s0, v0
	v_mfma_f32_16x16x32_bf16 a[0:3], v[18:21], v[6:9], a[0:3]
	ds_read_b128 v[18:21], v44 offset:61440
	v_mad_u32_u24 v1, v57, s2, v0
	v_add_u32_e32 v26, v1, v48
	v_mfma_f32_16x16x32_bf16 a[0:3], v[22:25], v[14:17], a[0:3]
	ds_read_b128 v[22:25], v44 offset:62464
	s_waitcnt lgkmcnt(1)
	v_mfma_f32_16x16x32_bf16 a[8:11], v[18:21], v[6:9], a[8:11]
	ds_read_b128 v[18:21], v44 offset:64512
	s_nop 3
	v_accvgpr_read_b32 v27, a1
	v_accvgpr_read_b32 v10, a0
	ds_write2_b32 v26, v10, v27 offset0:1 offset1:2
	v_accvgpr_read_b32 v10, a3
	v_accvgpr_read_b32 v11, a2
	ds_write2_b32 v26, v11, v10 offset0:3 offset1:4
	ds_read_b128 v[10:13], v44 offset:63488
	s_waitcnt lgkmcnt(4)
	v_mfma_f32_16x16x32_bf16 a[0:3], v[22:25], v[14:17], a[8:11]
	s_nop 7
	v_accvgpr_read_b32 v22, a1
	v_accvgpr_read_b32 v23, a0
	ds_write2_b32 v26, v23, v22 offset0:17 offset1:18
	v_or_b32_e32 v22, 0x10000, v44
	ds_read_b128 v[22:25], v22
	s_waitcnt lgkmcnt(2)
	v_mfma_f32_16x16x32_bf16 a[8:11], v[10:13], v[2:5], a[12:15]
	v_or_b32_e32 v10, 0x10400, v44
	ds_read_b128 v[10:13], v10
	v_accvgpr_read_b32 v27, a3
	v_mfma_f32_16x16x32_bf16 a[8:11], v[18:21], v[6:9], a[8:11]
	v_or_b32_e32 v18, 0x10800, v44
	ds_read_b128 v[18:21], v18
	v_accvgpr_read_b32 v28, a2
	s_waitcnt lgkmcnt(2)
	v_mfma_f32_16x16x32_bf16 a[0:3], v[22:25], v[14:17], a[8:11]
	v_or_b32_e32 v22, 0x10c00, v44
	ds_read_b128 v[22:25], v22
	ds_write2_b32 v26, v28, v27 offset0:19 offset1:20
	s_waitcnt lgkmcnt(3)
	v_mfma_f32_16x16x32_bf16 a[4:7], v[10:13], v[2:5], a[4:7]
	s_waitcnt lgkmcnt(2)
	v_mfma_f32_16x16x32_bf16 a[4:7], v[18:21], v[6:9], a[4:7]
	s_nop 0
	v_accvgpr_read_b32 v2, a1
	v_accvgpr_read_b32 v3, a0
	ds_write2_b32 v26, v3, v2 offset0:33 offset1:34
	v_accvgpr_read_b32 v2, a3
	v_accvgpr_read_b32 v3, a2
	s_waitcnt lgkmcnt(2)
	v_mfma_f32_16x16x32_bf16 a[0:3], v[22:25], v[14:17], a[4:7]
	ds_write2_b32 v26, v3, v2 offset0:35 offset1:36
	s_nop 6
	v_accvgpr_read_b32 v2, a1
	v_accvgpr_read_b32 v3, a0
	ds_write2_b32 v26, v3, v2 offset0:49 offset1:50
	v_accvgpr_read_b32 v2, a3
	v_accvgpr_read_b32 v3, a2
	ds_write2_b32 v26, v3, v2 offset0:51 offset1:52
	s_and_saveexec_b64 s[0:1], vcc
	ds_write_b32 v1, v46
	s_or_b64 exec, exec, s[0:1]
	v_add_u32_e32 v2, v0, v44
	v_mov_b64_e32 v[0:1], s[10:11]
	v_mad_u64_u32 v[0:1], s[0:1], v47, s2, v[0:1]
	ds_read_b128 v[4:7], v2
	v_lshl_add_u64 v[8:9], v[0:1], 0, v[44:45]
	s_waitcnt lgkmcnt(0)
	global_store_dwordx4 v[8:9], v[4:7], off sc1
	s_nop 1
	s_mov_b64 s[0:1], 0x400
	ds_read_b128 v[4:7], v2 offset:1024
	v_lshl_add_u64 v[10:11], v[8:9], 0, s[0:1]
	s_waitcnt lgkmcnt(0)
	global_store_dwordx4 v[10:11], v[4:7], off sc1
	s_nop 1
	s_mov_b64 s[0:1], 0x800
	ds_read_b128 v[4:7], v2 offset:2048
	v_lshl_add_u64 v[10:11], v[8:9], 0, s[0:1]
	s_waitcnt lgkmcnt(0)
	global_store_dwordx4 v[10:11], v[4:7], off sc1
	s_nop 1
	s_mov_b64 s[0:1], 0xc00
	ds_read_b128 v[4:7], v2 offset:3072
	v_lshl_add_u64 v[8:9], v[8:9], 0, s[0:1]
	s_waitcnt lgkmcnt(0)
	global_store_dwordx4 v[8:9], v[4:7], off sc1
	s_nop 1
	v_or_b32_e32 v3, 0x100, v49
	v_cmp_gt_u32_e32 vcc, s2, v3
	s_and_saveexec_b64 s[0:1], vcc
	s_cbranch_execz .LBB2_4
	ds_read_b128 v[4:7], v2 offset:4096
	v_lshlrev_b32_e32 v2, 4, v3
	v_mov_b32_e32 v3, 0
	v_lshl_add_u64 v[0:1], v[0:1], 0, v[2:3]
	s_waitcnt lgkmcnt(0)
	global_store_dwordx4 v[0:1], v[4:7], off sc1
	s_nop 1
